# MoE weight conversion moved into the GEMM1 tile epilogues of all 256 workgroups (no dedicated converter workgroups; 16 instead of 20 GEMM1 rounds in layers 0-2), on top of v017
# speedup vs baseline: 1.0065x; 1.0002x over previous
.LBB0_105:
	s_waitcnt lgkmcnt(0)
	s_lshr_b32 s4, s18, 6
	s_cmpk_lt_i32 s88, 0x900
	s_cselect_b64 s[0:1], -1, 0
	v_writelane_b32 v253, s0, 10
	s_ashr_i32 s97, s88, 31
	s_ashr_i32 s18, s96, 31
	v_writelane_b32 v253, s1, 11
	s_lshr_b32 s0, s97, 29
	s_add_i32 s0, s88, s0
	s_ashr_i32 s2, s0, 3
	s_and_b32 s0, s0, -8
	s_sub_i32 s3, s88, s0
	s_add_u32 s0, s16, 0x4200
	s_addc_u32 s1, s17, 0
	v_writelane_b32 v253, s0, 12
	v_mov_b32_e32 v207, 0
	v_mov_b32_e32 v252, 0x42000000
	v_writelane_b32 v253, s1, 13
	s_add_u32 s0, s16, 0x4400
	s_addc_u32 s1, s17, 0
	v_writelane_b32 v253, s0, 14
	v_mov_b64_e32 v[226:227], 0x200
	v_mov_b64_e32 v[250:251], 0x1ff
	v_writelane_b32 v253, s1, 15
	s_add_u32 s0, s16, 0x4500
	s_addc_u32 s1, s17, 0
	v_writelane_b32 v253, s0, 16
	s_mov_b32 s33, 0x43e00000
	s_nop 0
	v_writelane_b32 v253, s1, 17
	s_add_u32 s0, s16, 0x4600
	s_addc_u32 s1, s17, 0
	v_writelane_b32 v253, s0, 18
	s_nop 1
	v_writelane_b32 v253, s1, 19
	s_add_u32 s0, s16, 0x4700
	s_addc_u32 s1, s17, 0
	v_writelane_b32 v253, s0, 20
	s_nop 1
	v_writelane_b32 v253, s1, 21
	s_add_u32 s0, s16, 0x4800
	s_addc_u32 s1, s17, 0
	v_writelane_b32 v253, s0, 22
	s_nop 1
	v_writelane_b32 v253, s1, 23
	s_add_u32 s0, s16, 0x4900
	s_addc_u32 s1, s17, 0
	v_writelane_b32 v253, s0, 24
	s_nop 1
	v_writelane_b32 v253, s1, 25
	s_add_u32 s0, s16, 0x4a00
	s_addc_u32 s1, s17, 0
	v_writelane_b32 v253, s0, 26
	s_nop 1
	v_writelane_b32 v253, s1, 27
	s_add_u32 s0, s16, 0x4b00
	s_addc_u32 s1, s17, 0
	v_writelane_b32 v253, s0, 28
	s_nop 1
	v_writelane_b32 v253, s1, 29
	s_add_u32 s0, s16, 0x4c00
	s_addc_u32 s1, s17, 0
	v_writelane_b32 v253, s0, 30
	s_nop 1
	v_writelane_b32 v253, s1, 31
	s_add_u32 s0, s16, 0x4d00
	s_addc_u32 s1, s17, 0
	v_writelane_b32 v253, s0, 32
	s_nop 1
	v_writelane_b32 v253, s1, 33
	s_add_u32 s0, s16, 0x4e00
	s_addc_u32 s1, s17, 0
	v_writelane_b32 v253, s0, 34
	s_nop 1
	v_writelane_b32 v253, s1, 35
	s_add_u32 s0, s16, 0x4f00
	s_addc_u32 s1, s17, 0
	v_writelane_b32 v253, s0, 36
	s_nop 1
	v_writelane_b32 v253, s1, 37
	s_add_u32 s0, s16, 0x5000
	s_addc_u32 s1, s17, 0
	v_writelane_b32 v253, s0, 38
	s_nop 1
	v_writelane_b32 v253, s1, 39
	s_add_u32 s0, s16, 0x5100
	s_addc_u32 s1, s17, 0
	v_writelane_b32 v253, s0, 40
	s_nop 1
	v_writelane_b32 v253, s1, 41
	s_add_u32 s0, s16, 0x5200
	s_addc_u32 s1, s17, 0
	v_writelane_b32 v253, s0, 42
	s_nop 1
	v_writelane_b32 v253, s1, 43
	s_add_u32 s0, s16, 0x5300
	s_addc_u32 s1, s17, 0
	v_writelane_b32 v253, s0, 44
	s_cmp_eq_u32 s10, 15
	s_nop 0
	v_writelane_b32 v253, s1, 45
	s_cselect_b64 s[0:1], -1, 0
	v_writelane_b32 v253, s0, 46
	s_cmp_eq_u32 s10, 14
	s_nop 0
	v_writelane_b32 v253, s1, 47
	s_cselect_b64 s[0:1], -1, 0
	v_writelane_b32 v253, s0, 48
	s_cmp_eq_u32 s10, 13
	s_nop 0
	v_writelane_b32 v253, s1, 49
	s_cselect_b64 s[0:1], -1, 0
	v_writelane_b32 v253, s0, 50
	s_cmp_eq_u32 s10, 12
	s_nop 0
	v_writelane_b32 v253, s1, 51
	s_cselect_b64 s[0:1], -1, 0
	v_writelane_b32 v253, s0, 52
	s_cmp_eq_u32 s10, 11
	s_nop 0
	v_writelane_b32 v253, s1, 53
	s_cselect_b64 s[0:1], -1, 0
	v_writelane_b32 v253, s0, 54
	s_cmp_eq_u32 s10, 10
	s_nop 0
	v_writelane_b32 v253, s1, 55
	s_cselect_b64 s[0:1], -1, 0
	v_writelane_b32 v253, s0, 56
	s_cmp_eq_u32 s10, 9
	s_nop 0
	v_writelane_b32 v253, s1, 57
	s_cselect_b64 s[0:1], -1, 0
	v_writelane_b32 v253, s0, 58
	s_cmp_eq_u32 s10, 8
	s_nop 0
	v_writelane_b32 v253, s1, 59
	s_cselect_b64 s[0:1], -1, 0
	v_writelane_b32 v253, s0, 60
	s_cmp_eq_u32 s10, 7
	s_nop 0
	v_writelane_b32 v253, s1, 61
	s_cselect_b64 s[0:1], -1, 0
	v_writelane_b32 v253, s0, 62
	s_cmp_eq_u32 s10, 6
	s_nop 0
	v_writelane_b32 v253, s1, 63
	s_cselect_b64 s[0:1], -1, 0
	v_writelane_b32 v254, s0, 0
	s_cmp_eq_u32 s10, 5
	s_nop 0
	v_writelane_b32 v254, s1, 1
	s_cselect_b64 s[0:1], -1, 0
	v_writelane_b32 v254, s0, 2
	s_cmp_eq_u32 s10, 4
	s_nop 0
	v_writelane_b32 v254, s1, 3
	s_cselect_b64 s[0:1], -1, 0
	v_writelane_b32 v254, s0, 4
	s_cmp_eq_u32 s10, 3
	s_nop 0
	v_writelane_b32 v254, s1, 5
	s_cselect_b64 s[0:1], -1, 0
	v_writelane_b32 v254, s0, 6
	s_cmp_eq_u32 s10, 2
	s_nop 0
	v_writelane_b32 v254, s1, 7
	s_cselect_b64 s[0:1], -1, 0
	v_writelane_b32 v254, s0, 8
	s_cmp_eq_u32 s10, 1
	s_nop 0
	v_writelane_b32 v254, s1, 9
	s_cselect_b64 s[0:1], -1, 0
	v_writelane_b32 v254, s0, 10
	s_cmp_eq_u32 s10, 0
	s_nop 0
	v_writelane_b32 v254, s1, 11
	s_cselect_b64 s[0:1], -1, 0
	v_writelane_b32 v254, s0, 12
	s_nop 1
	v_writelane_b32 v254, s1, 13
	s_lshl_b32 s0, s10, 8
	s_add_u32 s0, s52, s0
	s_addc_u32 s1, s53, 0
	s_add_u32 s6, s0, 0x1400
	s_addc_u32 s7, s1, 0
	v_writelane_b32 v254, s6, 14
	s_add_u32 s0, s0, 0x2400
	s_addc_u32 s1, s1, 0
	v_writelane_b32 v254, s7, 15
	v_writelane_b32 v254, s0, 16
	s_mov_b32 s52, 0
	s_nop 0
	v_writelane_b32 v254, s1, 17
	s_add_u32 s0, s16, 0x7400
	s_addc_u32 s1, s17, 0
	v_writelane_b32 v254, s0, 18
	s_nop 1
	v_writelane_b32 v254, s1, 19
	s_add_u32 s0, s16, 0x7500
	s_addc_u32 s1, s17, 0
	v_writelane_b32 v254, s0, 20
	s_and_b32 s6, s96, 7
	s_nop 0
	v_writelane_b32 v254, s1, 21
	s_ashr_i32 s0, s96, 3
	s_mul_i32 s0, s0, s3
	s_add_i32 s7, s0, s2
	s_cmpk_lt_i32 s88, 0x200
	s_cselect_b64 s[0:1], -1, 0
	v_writelane_b32 v254, s0, 22
	s_nop 1
	v_writelane_b32 v254, s1, 23
	s_lshl_b32 s0, s3, 6
	s_cmpk_lt_i32 s88, 0x600
	s_cselect_b64 s[8:9], -1, 0
	v_writelane_b32 v254, s8, 24
	s_cmpk_lt_u32 s88, 0x800
	s_nop 0
	v_writelane_b32 v254, s9, 25
	s_cselect_b64 s[8:9], -1, 0
	s_lshl_b32 s1, s88, 4
	s_and_b32 s1, s1, 0x7f80
	v_writelane_b32 v254, s8, 26
	s_cmpk_lt_i32 s88, 0x800
	s_nop 0
	v_writelane_b32 v254, s9, 27
	s_cselect_b64 s[8:9], -1, 0
	v_writelane_b32 v254, s8, 28
	s_cmpk_lt_i32 s88, 0x80
	s_nop 0
	v_writelane_b32 v254, s9, 29
	s_cselect_b64 s[8:9], -1, 0
	v_writelane_b32 v254, s8, 30
	s_cmpk_gt_i32 s88, 0xff
	s_nop 0
	v_writelane_b32 v254, s9, 31
	s_cselect_b64 s[8:9], -1, 0
	v_writelane_b32 v254, s8, 32
	s_cmpk_lt_i32 s88, 0x1000
	s_nop 0
	v_writelane_b32 v254, s9, 33
	s_cselect_b64 s[8:9], -1, 0
	v_writelane_b32 v254, s8, 34
	s_and_b32 s5, s89, 8
	s_bfe_u32 s10, s88, 0x20003
	v_writelane_b32 v254, s9, 35
	s_bfe_u32 s8, s88, 0x30005
	s_lshl_b32 s9, s88, 1
	s_or_b32 s5, s5, s8
	s_ashr_i32 s8, s88, 4
	s_and_b32 s9, s9, 12
	s_and_b32 s8, s8, -16
	s_or_b32 s9, s9, s10
	s_or_b32 s9, s9, s8
	s_or_b32 s14, s5, s8
	v_writelane_b32 v254, s9, 36
	s_lshl_b32 s5, s9, 8
	v_writelane_b32 v254, s5, 37
	s_mov_b32 s12, s14
	s_ashr_i32 s15, s14, 31
	s_add_i32 s4, s4, s89
	v_writelane_b32 v254, s12, 38
	s_lshr_b32 s8, s88, 3
	s_add_i32 s5, s4, 0xfffff980
	v_writelane_b32 v254, s13, 39
	s_lshl_b64 s[12:13], s[14:15], 18
	v_writelane_b32 v254, s12, 40
	s_cmpk_lt_i32 s5, 0x6000
	s_nop 0
	v_writelane_b32 v254, s13, 41
	s_cselect_b64 s[12:13], -1, 0
	v_writelane_b32 v254, s12, 42
	s_cmpk_lt_i32 s88, 0x400
	s_nop 0
	v_writelane_b32 v254, s13, 43
	s_cselect_b64 s[12:13], -1, 0
	v_writelane_b32 v254, s12, 44
	s_ashr_i32 s9, s88, 6
	s_and_b32 s9, s9, -4
	v_writelane_b32 v254, s13, 45
	s_bfe_u32 s12, s88, 0x20001
	s_or_b32 s9, s12, s9
	s_lshl_b32 s12, s88, 5
	s_and_b32 s8, s8, 28
	s_and_b32 s12, s12, 32
	s_or_b32 s8, s12, s8
	s_lshr_b32 s8, s8, 2
	s_lshl_b32 s12, s9, 4
	s_or_b32 s12, s12, s8
	s_lshl_b32 s8, s9, 2
	s_or_b32 s14, s8, s10
	s_lshl_b32 s8, s96, 4
	v_writelane_b32 v254, s8, 46
	s_mov_b32 s8, s12
	s_ashr_i32 s13, s12, 31
	v_writelane_b32 v254, s8, 47
	s_ashr_i32 s15, s14, 31
	s_nop 0
	v_writelane_b32 v254, s9, 48
	s_lshl_b64 s[8:9], s[12:13], 19
	v_writelane_b32 v254, s8, 49
	s_nop 1
	v_writelane_b32 v254, s9, 50
	s_mov_b32 s8, s14
	v_writelane_b32 v254, s8, 51
	s_nop 1
	v_writelane_b32 v254, s9, 52
	s_lshl_b64 s[8:9], s[14:15], 19
	v_writelane_b32 v254, s8, 53
	s_cmp_lt_i32 s3, 0
	s_nop 0
	v_writelane_b32 v254, s9, 54
	s_mul_i32 s8, s3, 0x41
	s_cselect_b32 s8, s8, s0
	s_movk_i32 s0, 0x121
	s_cselect_b32 s0, s0, 0x120
	s_mul_i32 s0, s3, s0
	s_movk_i32 s9, 0xc1
	s_cselect_b32 s9, s9, 0xc0
	s_add_i32 s0, s0, s2
	s_mul_hi_i32 s10, s0, 0x38e38e39
	s_lshr_b32 s12, s10, 31
	s_ashr_i32 s10, s10, 5
	s_add_i32 s10, s10, s12
	s_mul_i32 s12, s10, 0x90
	s_sub_i32 s0, s0, s12
	s_bfe_u32 s12, s0, 0x3001c
	s_add_i32 s12, s0, s12
	s_and_b32 s13, s12, 0xfff8
	s_sub_i32 s0, s0, s13
	s_lshl_b32 s10, s10, 3
	s_sext_i32_i16 s12, s12
	s_sext_i32_i16 s0, s0
	s_add_i32 s16, s10, s0
	s_ashr_i32 s0, s12, 3
	v_writelane_b32 v254, s0, 55
	s_lshr_b32 s0, s12, 3
	s_cmp_eq_u32 s6, 0
	s_cselect_b32 s19, s7, s88
	s_cmpk_lt_i32 s19, 0xc00
	s_cselect_b64 s[6:7], -1, 0
	v_writelane_b32 v254, s6, 56
	s_mul_i32 s3, s3, s9
	s_nop 0
	v_writelane_b32 v254, s7, 57
	s_add_i32 s6, s8, s2
	s_ashr_i32 s7, s6, 31
	s_lshr_b32 s7, s7, 27
	s_add_i32 s7, s6, s7
	s_and_b32 s8, s7, 0xffe0
	s_add_i32 s2, s3, s2
	s_sub_i32 s6, s6, s8
	s_mul_hi_i32 s3, s2, 0x2aaaaaab
	s_bfe_i32 s8, s6, 0x80000
	s_lshr_b32 s9, s3, 31
	s_ashr_i32 s3, s3, 4
	s_bfe_u32 s8, s8, 0x3000c
	s_add_i32 s9, s3, s9
	s_add_i32 s8, s6, s8
	s_mul_i32 s3, s9, 0x60
	s_and_b32 s10, s8, 0xf8
	s_sub_i32 s3, s2, s3
	s_sub_i32 s6, s6, s10
	s_bfe_i32 s10, s3, 0x80000
	s_bfe_u32 s10, s10, 0x3000c
	s_add_i32 s10, s3, s10
	s_and_b32 s12, s10, 0xf8
	s_sub_i32 s12, s3, s12
	s_ashr_i32 s3, s2, 31
	s_lshr_b32 s3, s3, 22
	s_add_i32 s13, s2, s3
	s_and_b32 s3, s13, 0xfffffc00
	s_sub_i32 s14, s2, s3
	s_ashr_i32 s2, s19, 10
	s_lshl_b32 s17, s2, 1
	s_and_b32 s3, s19, 15
	s_lshl_b32 s15, -1, s17
	s_andn2_b32 s15, s3, s15
	s_lshr_b32 s3, s3, s17
	v_writelane_b32 v254, s15, 58
	s_lshl_b32 s15, s3, 8
	s_ashr_i32 s3, s2, 31
	s_lshl_b64 s[2:3], s[2:3], 24
	v_writelane_b32 v254, s2, 59
	v_cvt_f32_i32_e32 v1, s14
	s_nop 0
	v_writelane_b32 v254, s3, 60
	s_lshl_b32 s2, s19, 14
	s_and_b32 s2, s2, 0xfc0000
	v_writelane_b32 v254, s2, 61
	s_lshr_b32 s2, 0x1000, s17
	v_writelane_b32 v254, s17, 62
	s_add_i32 s2, s2, -1
	v_writelane_b32 v254, s2, 63
	s_ashr_i32 s2, s7, 5
	s_bfe_i32 s3, s8, 0x80000
	s_lshl_b32 s2, s2, 3
	s_sext_i32_i16 s7, s3
	s_sext_i32_i8 s3, s6
	s_add_i32 s20, s2, s3
	s_bfe_i32 s3, s10, 0x80000
	s_lshl_b32 s2, s9, 3
	s_sext_i32_i16 s3, s3
	s_sext_i32_i8 s6, s12
	s_add_i32 s22, s2, s6
	s_ashr_i32 s2, s3, 3
	v_writelane_b32 v255, s2, 0
	s_lshr_b32 s2, s3, 3
	s_bfe_i64 s[2:3], s[2:3], 0x100000
	s_lshl_b64 s[2:3], s[2:3], 19
	v_writelane_b32 v255, s2, 1
	s_ashr_i32 s23, s22, 31
	s_ashr_i32 s17, s16, 31
	v_writelane_b32 v255, s3, 2
	s_ashr_i32 s2, s13, 10
	s_lshl_b32 s6, s2, 3
	s_sub_i32 s2, 12, s6
	s_min_u32 s8, s2, 8
	s_bfe_i64 s[2:3], s[0:1], 0x100000
	s_lshl_b64 s[2:3], s[2:3], 18
	v_writelane_b32 v255, s2, 3
	s_ashr_i32 s0, s7, 3
	v_cvt_f32_ubyte0_e32 v2, s8
	v_writelane_b32 v255, s3, 4
	v_writelane_b32 v255, s0, 5
	s_lshr_b32 s0, s7, 3
	s_bfe_i64 s[2:3], s[0:1], 0x100000
	s_lshl_b64 s[2:3], s[2:3], 18
	v_writelane_b32 v255, s2, 6
	v_rcp_iflag_f32_e32 v3, v2
	s_ashr_i32 s21, s20, 31
	v_writelane_b32 v255, s3, 7
	v_writelane_b32 v255, s15, 8
	s_sub_i32 s2, s15, 64
	v_writelane_b32 v255, s2, 9
	s_mov_b32 s2, s22
	v_writelane_b32 v255, s2, 10
	v_mul_f32_e32 v3, v1, v3
	v_trunc_f32_e32 v3, v3
	v_writelane_b32 v255, s3, 11
	s_lshl_b64 s[2:3], s[22:23], 19
	v_writelane_b32 v255, s2, 12
	v_fma_f32 v1, -v3, v2, v1
	s_ashr_i32 s0, s14, 30
	v_writelane_b32 v255, s3, 13
	s_mov_b32 s2, s16
	v_writelane_b32 v255, s2, 14
	s_or_b32 s0, s0, 1
	s_mov_b32 s22, 0x3d000000
	v_writelane_b32 v255, s3, 15
	s_lshl_b64 s[2:3], s[16:17], 18
	v_writelane_b32 v255, s2, 16
	s_nop 1
	v_writelane_b32 v255, s3, 17
	s_mov_b32 s2, s20
	v_writelane_b32 v255, s2, 18
	s_nop 1
	v_writelane_b32 v255, s3, 19
	s_lshl_b64 s[2:3], s[20:21], 18
	v_writelane_b32 v255, s2, 20
	s_mov_b32 s21, 0x2aaaaaab
	s_movk_i32 s20, 0x110
	v_writelane_b32 v255, s3, 21
	v_cmp_ge_f32_e64 s[2:3], |v1|, v2
	v_cvt_i32_f32_e32 v1, v3
	s_and_b64 s[2:3], s[2:3], exec
	s_cselect_b32 s0, s0, 0
	v_readfirstlane_b32 s2, v1
	s_add_i32 s0, s2, s0
	s_mul_i32 s2, s0, s8
	s_sub_i32 s2, s14, s2
	s_sext_i32_i16 s2, s2
	s_add_i32 s6, s6, s2
	s_sext_i32_i16 s2, s0
	v_writelane_b32 v255, s2, 22
	s_bfe_i64 s[2:3], s[0:1], 0x100000
	s_lshl_b64 s[2:3], s[2:3], 19
	v_writelane_b32 v255, s2, 23
	s_mov_b32 s0, s6
	s_ashr_i32 s7, s6, 31
	v_writelane_b32 v255, s3, 24
	v_writelane_b32 v255, s0, 25
	s_lshl_b64 s[2:3], s[6:7], 19
	v_mov_b32_e32 v1, 0xff800000
	v_writelane_b32 v255, s1, 26
	v_writelane_b32 v255, s2, 27
	s_nop 1
	v_writelane_b32 v255, s3, 28
	s_add_u32 s2, s96, s88
	v_writelane_b32 v255, s18, 29
	s_addc_u32 s3, s18, s97
	v_writelane_b32 v255, s2, 30
	s_add_i32 s0, s96, s19
	s_lshl_b32 s0, s0, 14
	v_writelane_b32 v255, s3, 31
	v_writelane_b32 v255, s0, 32
	s_add_i32 s0, s4, 0xfffff800
	v_writelane_b32 v255, s0, 33
	s_lshl_b32 s0, s5, 6
	v_writelane_b32 v255, s0, 34
	s_lshl_b32 s0, s1, 2
	v_writelane_b32 v255, s0, 35
	v_writelane_b32 v255, s19, 36
	s_lshl_b32 s0, s19, 5
	v_writelane_b32 v255, s0, 37
	s_lshl_b32 s0, s96, 5
	v_writelane_b32 v255, s0, 38
	s_lshl_b32 s0, s96, 14
	v_writelane_b32 v255, s0, 39
	s_add_i32 s0, s90, s89
	v_writelane_b32 v255, s0, 40
	s_lshl_b32 s0, s88, 7
	v_writelane_b32 v255, s0, 41
	s_lshl_b32 s0, s96, 7
	v_writelane_b32 v255, s0, 42
	s_add_i32 s0, 0, 0x23f20
	v_writelane_b32 v255, s0, 43
	s_add_i32 s0, 0, 0x23f24
	s_ashr_i32 s91, s90, 31
	v_writelane_b32 v255, s0, 44
	s_add_i32 s0, 0, 0x20400
	v_writelane_b32 v255, s0, 45
	s_lshl_b64 s[0:1], s[90:91], 10
	v_writelane_b32 v255, s0, 46
	s_brev_b32 s2, -2
	s_movk_i32 s3, 0x1800
	v_writelane_b32 v255, s1, 47
	s_lshl_b64 s[0:1], s[90:91], 5
	v_writelane_b32 v255, s0, 48
	s_movk_i32 s19, 0x610
	s_nop 0
	v_writelane_b32 v255, s1, 49
	v_writelane_b32 v255, s88, 50
	v_writelane_b32 v255, s89, 51
	s_branch .LBB0_109

.LBB0_1240:
	s_add_u32 s50, s40, 0x47e00000
	s_addc_u32 s51, s41, 0
	s_and_b64 s[0:1], s[0:1], exec
	s_cselect_b32 s27, 0x100, s96
	s_add_u32 s0, s74, 0x80
	s_addc_u32 s1, s75, 0
	s_add_i32 s28, s10, 0x18000
	v_mov_b32_e32 v4, v194
	s_waitcnt vmcnt(2)
	s_barrier
	s_mov_b32 m0, s28
	v_add_u32_e32 v199, 0, v3
	global_load_lds_dwordx4 v4, s[0:1]
	s_add_u32 s0, s74, 0x20080
	s_addc_u32 s1, s75, 0
	s_add_i32 s29, s10, 0x1a000
	v_mov_b32_e32 v4, v194
	s_add_u32 s52, s42, 0x80
	s_mov_b32 m0, s29
	s_addc_u32 s53, s43, 0
	global_load_lds_dwordx4 v4, s[0:1]
	s_mov_b64 s[0:1], s[52:53]
	v_mov_b32_e32 v4, v195
	s_add_i32 s30, s10, 0x8000
	s_mov_b32 m0, s30
	s_add_i32 s31, s10, 0xa000
	global_load_lds_dwordx4 v4, s[0:1]
	v_mov_b32_e32 v4, v196
	s_mov_b32 m0, s31
	s_add_i32 s34, s10, 0x1c000
	s_mov_b32 s82, 0
	global_load_lds_dwordx4 v4, s[0:1]
	s_add_u32 s0, s74, 0x8080
	s_addc_u32 s1, s75, 0
	v_mov_b32_e32 v4, v194
	s_mov_b32 m0, s34
	v_add_u32_e32 v200, 0, v2
	global_load_lds_dwordx4 v4, s[0:1]
	s_add_u32 s0, s74, 0x28080
	s_addc_u32 s1, s75, 0
	s_add_i32 s35, s10, 0x1e000
	v_mov_b32_e32 v4, v194
	s_mov_b32 m0, s35
	s_cmp_gt_i32 s24, 3
	global_load_lds_dwordx4 v4, s[0:1]
	s_cselect_b64 s[54:55], -1, 0
	s_lshl_b32 s36, s24, 8
	v_readlane_b32 s1, v255, 45
	s_add_i32 s37, s1, s36
	s_cmp_lt_i32 s24, 4
	s_cselect_b64 s[56:57], -1, 0
	s_cmpk_lt_u32 s23, 0x100
	s_cselect_b64 s[58:59], -1, 0
	s_add_u32 s60, s42, 0x100
	s_addc_u32 s61, s43, 0
	s_add_u32 s62, s42, 0x180
	s_addc_u32 s63, s43, 0
	s_add_u32 s64, s42, 0x200
	s_addc_u32 s65, s43, 0
	s_add_u32 s66, s42, 0x280
	s_addc_u32 s67, s43, 0
	s_add_u32 s68, s42, 0x300
	s_addc_u32 s69, s43, 0
	s_add_u32 s70, s42, 0x380
	s_waitcnt vmcnt(6)
	s_addc_u32 s71, s43, 0
	s_lshl_b32 s0, s7, 2
	s_add_i32 s76, s1, s0
	s_add_i32 s77, s88, s27
	v_readlane_b32 s0, v254, 38
	s_lshl_b32 s78, s77, 1
	s_lshl_b32 s79, s27, 1
	s_lshl_b32 s80, s77, 3
	s_lshl_b32 s81, s27, 3
	v_readlane_b32 s85, v254, 36
	s_mov_b32 s84, s0
	s_barrier
	v_readlane_b32 s1, v254, 39
	s_branch .LBB0_1243

.LBB0_1251:
	s_mov_b32 s100, -1
	v_readlane_b32 s23, v255, 55
	s_lshr_b32 s73, s77, 8
	s_cmp_lt_u32 s23, 3
	s_cbranch_scc0 .Lfz_s_skip
	s_cmp_le_u32 s73, 12
	s_cbranch_scc0 .Lfz_s_skip
	s_add_i32 s73, s73, -1
	s_lshl_b32 s73, s73, 11
	s_lshl_b32 s74, s88, 3
	s_add_i32 s73, s73, s74
	v_lshrrev_b32_e32 v224, 6, v0
	v_readlane_b32 s4, v253, 0
	v_readlane_b32 s5, v253, 1
	v_readfirstlane_b32 s74, v224
	s_add_i32 s100, s73, s74
	s_lshr_b32 s73, s100, 9
	s_mul_i32 s74, s73, 0xaaab
	s_lshr_b32 s74, s74, 17
	s_mul_i32 s75, s74, 3
	s_sub_i32 s73, s73, s75
	s_add_i32 s23, s23, 1
	s_lshl_b32 s23, s23, 4
	s_add_i32 s23, s23, s74
	s_lshl_b32 s75, s73, 3
	s_add_i32 s75, s75, 0x80
	s_load_dwordx2 s[4:5], s[4:5], s75
	s_and_b32 s74, s100, 0x1ff
	s_lshr_b32 s75, s74, 5
	s_lshl_b32 s75, s75, 19
	s_and_b32 s101, s74, 31
	s_lshl_b32 s101, s101, 8
	s_or_b32 s75, s75, s101
	s_lshr_b32 s101, s74, 4
	s_lshl_b32 s101, s101, 18
	s_and_b32 s74, s74, 15
	s_lshl_b32 s74, s74, 8
	s_or_b32 s74, s74, s101
	s_cmp_lt_u32 s73, 2
	s_cselect_b32 s75, s75, s74
	s_cselect_b32 s101, 17, 16
	s_mov_b32 s73, 0x1000
	s_cselect_b32 s73, 0x2000, s73
	s_lshl_b32 s74, s23, 23
	s_add_u32 s75, s75, s74
	v_bfe_u32 v224, v0, 4, 2
	v_and_b32_e32 v225, 15, v0
	v_lshlrev_b32_e32 v224, s101, v224
	v_lshl_or_b32 v201, v225, 4, v224
	s_waitcnt lgkmcnt(0)
	s_add_u32 s4, s4, s75
	s_addc_u32 s5, s5, 0
	global_load_dwordx4 v[134:137], v201, s[4:5] nt
	s_add_u32 s4, s4, s73
	s_addc_u32 s5, s5, 0
	global_load_dwordx4 v[138:141], v201, s[4:5] nt
	s_add_u32 s4, s4, s73
	s_addc_u32 s5, s5, 0
	global_load_dwordx4 v[142:145], v201, s[4:5] nt
	s_add_u32 s4, s4, s73
	s_addc_u32 s5, s5, 0
	global_load_dwordx4 v[146:149], v201, s[4:5] nt
	s_add_u32 s4, s4, s73
	s_addc_u32 s5, s5, 0
	global_load_dwordx4 v[150:153], v201, s[4:5] nt
	s_add_u32 s4, s4, s73
	s_addc_u32 s5, s5, 0
	global_load_dwordx4 v[154:157], v201, s[4:5] nt
	s_add_u32 s4, s4, s73
	s_addc_u32 s5, s5, 0
	global_load_dwordx4 v[158:161], v201, s[4:5] nt
	s_add_u32 s4, s4, s73
	s_addc_u32 s5, s5, 0
	global_load_dwordx4 v[162:165], v201, s[4:5] nt
	s_add_u32 s4, s4, s73
	s_addc_u32 s5, s5, 0
	global_load_dwordx4 v[166:169], v201, s[4:5] nt
	s_add_u32 s4, s4, s73
	s_addc_u32 s5, s5, 0
	global_load_dwordx4 v[186:189], v201, s[4:5] nt
	s_add_u32 s4, s4, s73
	s_addc_u32 s5, s5, 0
	global_load_dwordx4 v[190:193], v201, s[4:5] nt
	s_add_u32 s4, s4, s73
	s_addc_u32 s5, s5, 0
	global_load_dwordx4 v[208:211], v201, s[4:5] nt
	s_add_u32 s4, s4, s73
	s_addc_u32 s5, s5, 0
	global_load_dwordx4 v[212:215], v201, s[4:5] nt
	s_add_u32 s4, s4, s73
	s_addc_u32 s5, s5, 0
	global_load_dwordx4 v[216:219], v201, s[4:5] nt
	s_add_u32 s4, s4, s73
	s_addc_u32 s5, s5, 0
	global_load_dwordx4 v[220:223], v201, s[4:5] nt
	s_add_u32 s4, s4, s73
	s_addc_u32 s5, s5, 0
	global_load_dwordx4 v[234:237], v201, s[4:5] nt
.Lfz_s_skip:
	s_nop 0
	v_mov_b32_e32 v56, v0
	s_and_b32 s1, s82, 0x400
	s_lshl_b32 s0, s85, 8
	v_and_b32_e32 v54, 15, v56
	s_add_i32 s1, s76, s1
	s_add_i32 s0, s0, s7
	v_lshl_add_u32 v132, v54, 2, s1
	v_or_b32_e32 v130, s0, v54
	ds_read2_b32 v[54:55], v132 offset1:16
	s_lshl_b32 s0, s84, 7
	s_and_b32 s0, s0, 0x780
	v_lshrrev_b32_e32 v56, 1, v56
	v_and_or_b32 v56, v56, 24, s0
	s_waitcnt lgkmcnt(0)
	v_mul_f32_e32 v54, 0x3b800000, v54
	v_pk_mul_f32 v[62:63], v[122:123], v[54:55] op_sel_hi:[1,0]
	v_pk_mul_f32 v[86:87], v[118:119], v[54:55] op_sel_hi:[1,0]
	v_mul_f32_e32 v92, 0xbfb8aa3b, v62
	v_exp_f32_e32 v118, v92
	v_pk_mul_f32 v[92:93], v[116:117], v[54:55] op_sel_hi:[1,0]
	v_mul_f32_e32 v116, 0xbfb8aa3b, v63
	v_exp_f32_e32 v116, v116
	v_or_b32_e32 v206, s6, v56
	v_pk_mul_f32 v[56:57], v[124:125], v[54:55] op_sel_hi:[1,0]
	v_pk_mul_f32 v[64:65], v[120:121], v[54:55] op_sel_hi:[1,0]
	v_pk_mul_f32 v[88:89], v[128:129], v[54:55] op_sel_hi:[1,0]
	v_pk_mul_f32 v[90:91], v[126:127], v[54:55] op_sel_hi:[1,0]
	v_add_f32_e32 v117, 1.0, v118
	v_pk_mul_f32 v[114:115], v[114:115], v[54:55] op_sel_hi:[1,0]
	v_add_f32_e32 v54, 1.0, v116
	v_rcp_f32_e32 v117, v117
	v_rcp_f32_e32 v54, v54
	v_ashrrev_i32_e32 v131, 31, v130
	s_mov_b32 s0, 0x40000
	v_mul_f32_e32 v62, v62, v117
	v_mul_f32_e32 v54, v63, v54
	v_mul_f32_e32 v63, 0xbfb8aa3b, v56
	v_mul_f32_e32 v62, v90, v62
	v_exp_f32_e32 v63, v63
	v_mul_f32_e32 v90, 0xbfb8aa3b, v57
	v_exp_f32_e32 v90, v90
	v_mul_f32_e32 v62, 0x41000000, v62
	v_add_f32_e32 v63, 1.0, v63
	v_rcp_f32_e32 v63, v63
	v_add_f32_e32 v90, 1.0, v90
	v_rcp_f32_e32 v90, v90
	v_mul_f32_e32 v54, v91, v54
	v_mul_f32_e32 v56, v56, v63
	v_mul_f32_e32 v54, 0x41000000, v54
	v_mul_f32_e32 v56, v88, v56
	v_mul_f32_e32 v57, v57, v90
	v_min_f32_e64 v63, |v62|, s33
	v_mul_f32_e32 v88, 0xbfb8aa3b, v86
	v_mul_f32_e32 v56, 0x41000000, v56
	v_mul_f32_e32 v57, v89, v57
	v_bfi_b32 v62, s2, v63, v62
	v_min_f32_e64 v63, |v54|, s33
	v_exp_f32_e32 v88, v88
	v_mul_f32_e32 v57, 0x41000000, v57
	v_bfi_b32 v54, s2, v63, v54
	v_min_f32_e64 v63, |v56|, s33
	v_bfi_b32 v63, s2, v63, v56
	v_min_f32_e64 v56, |v57|, s33
	v_bfi_b32 v57, s2, v56, v57
	v_mov_b32_e32 v56, v207
	v_cvt_pk_fp8_f32 v56, v62, v54
	v_add_f32_e32 v62, 1.0, v88
	v_rcp_f32_e32 v62, v62
	v_mul_f32_e32 v54, 0xbfb8aa3b, v87
	v_exp_f32_e32 v54, v54
	v_cvt_pk_fp8_f32 v56, v63, v57 op_sel:[0,0,1]
	v_mul_f32_e32 v57, v86, v62
	v_mul_f32_e32 v62, 0xbfb8aa3b, v64
	v_exp_f32_e32 v62, v62
	v_mul_f32_e32 v63, 0xbfb8aa3b, v65
	v_add_f32_e32 v54, 1.0, v54
	v_exp_f32_e32 v63, v63
	v_rcp_f32_e32 v54, v54
	v_add_f32_e32 v62, 1.0, v62
	v_rcp_f32_e32 v62, v62
	v_add_f32_e32 v63, 1.0, v63
	v_mul_f32_e32 v57, v114, v57
	v_mul_f32_e32 v54, v87, v54
	v_rcp_f32_e32 v63, v63
	v_mul_f32_e32 v57, 0x41000000, v57
	v_mul_f32_e32 v54, v115, v54
	v_mul_f32_e32 v54, 0x41000000, v54
	v_mul_f32_e32 v62, v64, v62
	v_min_f32_e64 v64, |v57|, s33
	v_bfi_b32 v64, s2, v64, v57
	v_min_f32_e64 v57, |v54|, s33
	v_mul_f32_e32 v62, v92, v62
	v_mul_f32_e32 v63, v65, v63
	v_bfi_b32 v54, s2, v57, v54
	v_mov_b32_e32 v57, v207
	v_mul_f32_e32 v62, 0x41000000, v62
	v_mul_f32_e32 v63, v93, v63
	v_cvt_pk_fp8_f32 v57, v64, v54
	v_mul_f32_e32 v63, 0x41000000, v63
	v_min_f32_e64 v65, |v62|, s33
	v_bfi_b32 v54, s2, v65, v62
	v_min_f32_e64 v62, |v63|, s33
	v_bfi_b32 v62, s2, v62, v63
	v_cvt_pk_fp8_f32 v57, v54, v62 op_sel:[0,0,1]
	v_lshlrev_b64 v[62:63], 11, v[130:131]
	v_mul_f32_e32 v54, 0x3b800000, v55
	v_lshl_add_u64 v[62:63], s[50:51], 0, v[62:63]
	v_pk_mul_f32 v[64:65], v[106:107], v[54:55] op_sel_hi:[1,0]
	v_lshl_add_u64 v[114:115], v[62:63], 0, v[206:207]
	v_pk_mul_f32 v[62:63], v[108:109], v[54:55] op_sel_hi:[1,0]
	v_pk_mul_f32 v[86:87], v[104:105], v[54:55] op_sel_hi:[1,0]
	v_pk_mul_f32 v[88:89], v[102:103], v[54:55] op_sel_hi:[1,0]
	v_pk_mul_f32 v[90:91], v[112:113], v[54:55] op_sel_hi:[1,0]
	v_pk_mul_f32 v[92:93], v[110:111], v[54:55] op_sel_hi:[1,0]
	v_mul_f32_e32 v55, 0xbfb8aa3b, v64
	v_exp_f32_e32 v55, v55
	v_mul_f32_e32 v102, 0xbfb8aa3b, v65
	v_exp_f32_e32 v102, v102
	global_store_dwordx2 v[114:115], v[56:57], off
	v_pk_mul_f32 v[100:101], v[100:101], v[54:55] op_sel_hi:[1,0]
	v_add_f32_e32 v55, 1.0, v55
	v_rcp_f32_e32 v103, v55
	v_pk_mul_f32 v[54:55], v[98:99], v[54:55] op_sel_hi:[1,0]
	v_add_f32_e32 v98, 1.0, v102
	v_rcp_f32_e32 v98, v98
	v_mul_f32_e32 v64, v64, v103
	v_mul_f32_e32 v64, v92, v64
	v_mul_f32_e32 v92, 0xbfb8aa3b, v62
	v_mul_f32_e32 v65, v65, v98
	v_exp_f32_e32 v92, v92
	v_mul_f32_e32 v65, v93, v65
	v_mul_f32_e32 v93, 0xbfb8aa3b, v63
	v_exp_f32_e32 v93, v93
	v_add_f32_e32 v92, 1.0, v92
	v_rcp_f32_e32 v92, v92
	v_mul_f32_e32 v64, 0x41000000, v64
	v_add_f32_e32 v93, 1.0, v93
	v_rcp_f32_e32 v93, v93
	v_mul_f32_e32 v62, v62, v92
	v_mul_f32_e32 v65, 0x41000000, v65
	v_mul_f32_e32 v62, v90, v62
	v_mul_f32_e32 v63, v63, v93
	v_min_f32_e64 v90, |v64|, s33
	v_mul_f32_e32 v62, 0x41000000, v62
	v_mul_f32_e32 v63, v91, v63
	v_bfi_b32 v64, s2, v90, v64
	v_min_f32_e64 v90, |v65|, s33
	v_mul_f32_e32 v63, 0x41000000, v63
	v_bfi_b32 v65, s2, v90, v65
	v_min_f32_e64 v90, |v62|, s33
	v_bfi_b32 v90, s2, v90, v62
	v_min_f32_e64 v62, |v63|, s33
	v_bfi_b32 v63, s2, v62, v63
	v_mov_b32_e32 v62, v207
	v_cvt_pk_fp8_f32 v62, v64, v65
	v_mul_f32_e32 v64, 0xbfb8aa3b, v89
	v_exp_f32_e32 v64, v64
	v_mul_f32_e32 v91, 0xbfb8aa3b, v88
	v_exp_f32_e32 v91, v91
	v_cvt_pk_fp8_f32 v62, v90, v63 op_sel:[0,0,1]
	v_add_f32_e32 v63, 1.0, v64
	v_rcp_f32_e32 v63, v63
	v_add_f32_e32 v65, 1.0, v91
	v_rcp_f32_e32 v65, v65
	v_or_b32_e32 v56, 16, v130
	v_mul_f32_e32 v63, v89, v63
	v_mul_f32_e32 v55, v55, v63
	v_mul_f32_e32 v63, 0xbfb8aa3b, v87
	v_exp_f32_e32 v63, v63
	v_mul_f32_e32 v64, v88, v65
	v_mul_f32_e32 v54, v54, v64
	v_mul_f32_e32 v64, 0xbfb8aa3b, v86
	v_exp_f32_e32 v64, v64
	v_add_f32_e32 v63, 1.0, v63
	v_rcp_f32_e32 v63, v63
	v_mul_f32_e32 v54, 0x41000000, v54
	v_add_f32_e32 v64, 1.0, v64
	v_rcp_f32_e32 v64, v64
	v_mul_f32_e32 v63, v87, v63
	v_mul_f32_e32 v63, v101, v63
	v_mul_f32_e32 v55, 0x41000000, v55
	v_mul_f32_e32 v65, 0x41000000, v63
	v_min_f32_e64 v63, |v54|, s33
	v_bfi_b32 v54, s2, v63, v54
	v_min_f32_e64 v63, |v55|, s33
	v_mul_f32_e32 v64, v86, v64
	v_bfi_b32 v55, s2, v63, v55
	v_mov_b32_e32 v63, v207
	v_mul_f32_e32 v64, v100, v64
	v_cvt_pk_fp8_f32 v63, v54, v55
	v_mul_f32_e32 v64, 0x41000000, v64
	v_ashrrev_i32_e32 v57, 31, v56
	v_min_f32_e64 v86, |v64|, s33
	v_min_f32_e64 v55, |v65|, s33
	v_lshlrev_b64 v[56:57], 11, v[56:57]
	v_bfi_b32 v54, s2, v86, v64
	v_bfi_b32 v55, s2, v55, v65
	v_cvt_pk_fp8_f32 v63, v54, v55 op_sel:[0,0,1]
	v_lshl_add_u64 v[54:55], s[50:51], 0, v[56:57]
	ds_read2_b32 v[56:57], v132 offset0:32 offset1:48
	v_lshl_add_u64 v[54:55], v[54:55], 0, v[206:207]
	global_store_dwordx2 v[54:55], v[62:63], off
	v_or_b32_e32 v54, 32, v130
	v_ashrrev_i32_e32 v55, 31, v54
	s_waitcnt lgkmcnt(0)
	v_mul_f32_e32 v56, 0x3b800000, v56
	v_pk_mul_f32 v[58:59], v[58:59], v[56:57] op_sel_hi:[1,0]
	v_pk_mul_f32 v[60:61], v[60:61], v[56:57] op_sel_hi:[1,0]
	v_mul_f32_e32 v86, 0xbfb8aa3b, v58
	v_mul_f32_e32 v87, 0xbfb8aa3b, v59
	v_exp_f32_e32 v86, v86
	v_exp_f32_e32 v87, v87
	v_pk_mul_f32 v[12:13], v[12:13], v[56:57] op_sel_hi:[1,0]
	v_pk_mul_f32 v[10:11], v[10:11], v[56:57] op_sel_hi:[1,0]
	v_pk_mul_f32 v[62:63], v[96:97], v[56:57] op_sel_hi:[1,0]
	v_pk_mul_f32 v[64:65], v[94:95], v[56:57] op_sel_hi:[1,0]
	v_pk_mul_f32 v[84:85], v[84:85], v[56:57] op_sel_hi:[1,0]
	v_add_f32_e32 v86, 1.0, v86
	v_pk_mul_f32 v[82:83], v[82:83], v[56:57] op_sel_hi:[1,0]
	v_add_f32_e32 v56, 1.0, v87
	v_rcp_f32_e32 v86, v86
	v_rcp_f32_e32 v56, v56
	v_mov_b64_e32 v[226:227], v[250:251]
	v_mov_b64_e32 v[250:251], v[232:233]
	v_mul_f32_e32 v58, v58, v86
	v_mul_f32_e32 v56, v59, v56
	v_mul_f32_e32 v59, 0xbfb8aa3b, v60
	v_mul_f32_e32 v58, v64, v58
	v_exp_f32_e32 v59, v59
	v_mul_f32_e32 v64, 0xbfb8aa3b, v61
	v_exp_f32_e32 v64, v64
	v_mul_f32_e32 v58, 0x41000000, v58
	v_add_f32_e32 v59, 1.0, v59
	v_rcp_f32_e32 v59, v59
	v_add_f32_e32 v64, 1.0, v64
	v_rcp_f32_e32 v64, v64
	v_mul_f32_e32 v56, v65, v56
	v_mul_f32_e32 v59, v60, v59
	v_mul_f32_e32 v56, 0x41000000, v56
	v_mul_f32_e32 v59, v62, v59
	v_mul_f32_e32 v60, v61, v64
	v_min_f32_e64 v61, |v58|, s33
	v_mul_f32_e32 v59, 0x41000000, v59
	v_mul_f32_e32 v60, v63, v60
	v_bfi_b32 v61, s2, v61, v58
	v_min_f32_e64 v58, |v56|, s33
	v_mul_f32_e32 v60, 0x41000000, v60
	v_bfi_b32 v56, s2, v58, v56
	v_min_f32_e64 v58, |v59|, s33
	v_bfi_b32 v59, s2, v58, v59
	v_min_f32_e64 v58, |v60|, s33
	v_bfi_b32 v60, s2, v58, v60
	v_mov_b32_e32 v58, v207
	v_cvt_pk_fp8_f32 v58, v61, v56
	v_mul_f32_e32 v56, 0xbfb8aa3b, v11
	v_exp_f32_e32 v56, v56
	v_mul_f32_e32 v62, 0xbfb8aa3b, v10
	v_exp_f32_e32 v62, v62
	v_cvt_pk_fp8_f32 v58, v59, v60 op_sel:[0,0,1]
	v_add_f32_e32 v56, 1.0, v56
	v_rcp_f32_e32 v56, v56
	v_add_f32_e32 v61, 1.0, v62
	v_mul_f32_e32 v59, 0xbfb8aa3b, v13
	v_rcp_f32_e32 v61, v61
	v_mul_f32_e32 v11, v11, v56
	v_mul_f32_e32 v56, 0xbfb8aa3b, v12
	v_exp_f32_e32 v56, v56
	v_exp_f32_e32 v59, v59
	v_mul_f32_e32 v10, v10, v61
	v_mul_f32_e32 v10, v82, v10
	v_add_f32_e32 v56, 1.0, v56
	v_rcp_f32_e32 v56, v56
	v_add_f32_e32 v59, 1.0, v59
	v_rcp_f32_e32 v59, v59
	v_mul_f32_e32 v10, 0x41000000, v10
	v_mul_f32_e32 v11, v83, v11
	v_mul_f32_e32 v11, 0x41000000, v11
	v_mul_f32_e32 v12, v12, v56
	v_min_f32_e64 v56, |v10|, s33
	v_bfi_b32 v10, s2, v56, v10
	v_min_f32_e64 v56, |v11|, s33
	v_mul_f32_e32 v13, v13, v59
	v_bfi_b32 v11, s2, v56, v11
	v_mov_b32_e32 v59, v207
	v_mul_f32_e32 v12, v84, v12
	v_mul_f32_e32 v13, v85, v13
	v_cvt_pk_fp8_f32 v59, v10, v11
	v_mul_f32_e32 v12, 0x41000000, v12
	v_mul_f32_e32 v13, 0x41000000, v13
	v_min_f32_e64 v56, |v12|, s33
	v_min_f32_e64 v11, |v13|, s33
	v_bfi_b32 v10, s2, v56, v12
	v_bfi_b32 v11, s2, v11, v13
	v_cvt_pk_fp8_f32 v59, v10, v11 op_sel:[0,0,1]
	v_lshlrev_b64 v[10:11], 11, v[54:55]
	v_lshl_add_u64 v[10:11], s[50:51], 0, v[10:11]
	v_mul_f32_e32 v12, 0x3b800000, v57
	v_lshl_add_u64 v[10:11], v[10:11], 0, v[206:207]
	v_pk_mul_f32 v[56:57], v[74:75], v[12:13] op_sel_hi:[1,0]
	global_store_dwordx2 v[10:11], v[58:59], off
	v_pk_mul_f32 v[54:55], v[76:77], v[12:13] op_sel_hi:[1,0]
	v_pk_mul_f32 v[58:59], v[72:73], v[12:13] op_sel_hi:[1,0]
	v_pk_mul_f32 v[60:61], v[70:71], v[12:13] op_sel_hi:[1,0]
	v_pk_mul_f32 v[62:63], v[80:81], v[12:13] op_sel_hi:[1,0]
	v_pk_mul_f32 v[64:65], v[78:79], v[12:13] op_sel_hi:[1,0]
	v_mul_f32_e32 v13, 0xbfb8aa3b, v56
	v_exp_f32_e32 v13, v13
	v_mul_f32_e32 v70, 0xbfb8aa3b, v57
	v_exp_f32_e32 v70, v70
	v_or_b32_e32 v10, 48, v130
	v_pk_mul_f32 v[68:69], v[68:69], v[12:13] op_sel_hi:[1,0]
	v_add_f32_e32 v13, 1.0, v13
	v_rcp_f32_e32 v71, v13
	v_pk_mul_f32 v[12:13], v[66:67], v[12:13] op_sel_hi:[1,0]
	v_add_f32_e32 v66, 1.0, v70
	v_rcp_f32_e32 v66, v66
	v_mul_f32_e32 v56, v56, v71
	v_mul_f32_e32 v56, v64, v56
	v_mul_f32_e32 v64, 0xbfb8aa3b, v54
	v_mul_f32_e32 v57, v57, v66
	v_exp_f32_e32 v64, v64
	v_mul_f32_e32 v57, v65, v57
	v_mul_f32_e32 v65, 0xbfb8aa3b, v55
	v_exp_f32_e32 v65, v65
	v_add_f32_e32 v64, 1.0, v64
	v_rcp_f32_e32 v64, v64
	v_mul_f32_e32 v56, 0x41000000, v56
	v_add_f32_e32 v65, 1.0, v65
	v_rcp_f32_e32 v65, v65
	v_mul_f32_e32 v54, v54, v64
	v_mul_f32_e32 v57, 0x41000000, v57
	v_mul_f32_e32 v54, v62, v54
	v_mul_f32_e32 v55, v55, v65
	v_min_f32_e64 v62, |v56|, s33
	v_mul_f32_e32 v54, 0x41000000, v54
	v_mul_f32_e32 v55, v63, v55
	v_bfi_b32 v56, s2, v62, v56
	v_min_f32_e64 v62, |v57|, s33
	v_mul_f32_e32 v55, 0x41000000, v55
	v_bfi_b32 v57, s2, v62, v57
	v_min_f32_e64 v62, |v54|, s33
	v_bfi_b32 v62, s2, v62, v54
	v_min_f32_e64 v54, |v55|, s33
	v_bfi_b32 v55, s2, v54, v55
	v_mov_b32_e32 v54, v207
	v_cvt_pk_fp8_f32 v54, v56, v57
	v_mul_f32_e32 v56, 0xbfb8aa3b, v61
	v_exp_f32_e32 v56, v56
	v_mul_f32_e32 v63, 0xbfb8aa3b, v60
	v_exp_f32_e32 v63, v63
	v_cvt_pk_fp8_f32 v54, v62, v55 op_sel:[0,0,1]
	v_add_f32_e32 v55, 1.0, v56
	v_rcp_f32_e32 v55, v55
	v_add_f32_e32 v57, 1.0, v63
	v_rcp_f32_e32 v57, v57
	v_ashrrev_i32_e32 v11, 31, v10
	v_mul_f32_e32 v55, v61, v55
	v_mul_f32_e32 v13, v13, v55
	v_mul_f32_e32 v55, 0xbfb8aa3b, v59
	v_exp_f32_e32 v55, v55
	v_mul_f32_e32 v56, v60, v57
	v_mul_f32_e32 v12, v12, v56
	v_mul_f32_e32 v56, 0xbfb8aa3b, v58
	v_exp_f32_e32 v56, v56
	v_add_f32_e32 v55, 1.0, v55
	v_rcp_f32_e32 v55, v55
	v_mul_f32_e32 v12, 0x41000000, v12
	v_add_f32_e32 v56, 1.0, v56
	v_rcp_f32_e32 v56, v56
	v_mul_f32_e32 v55, v59, v55
	v_mul_f32_e32 v55, v69, v55
	v_mul_f32_e32 v13, 0x41000000, v13
	v_mul_f32_e32 v57, 0x41000000, v55
	v_min_f32_e64 v55, |v12|, s33
	v_bfi_b32 v12, s2, v55, v12
	v_min_f32_e64 v55, |v13|, s33
	v_mul_f32_e32 v56, v58, v56
	v_bfi_b32 v13, s2, v55, v13
	v_mov_b32_e32 v55, v207
	v_mul_f32_e32 v56, v68, v56
	v_cvt_pk_fp8_f32 v55, v12, v13
	v_mul_f32_e32 v56, 0x41000000, v56
	v_min_f32_e64 v58, |v56|, s33
	v_min_f32_e64 v13, |v57|, s33
	v_bfi_b32 v12, s2, v58, v56
	v_bfi_b32 v13, s2, v13, v57
	v_cvt_pk_fp8_f32 v55, v12, v13 op_sel:[0,0,1]
	ds_read2_b32 v[12:13], v132 offset0:128 offset1:144
	v_lshlrev_b64 v[10:11], 11, v[10:11]
	v_lshl_add_u64 v[10:11], s[50:51], 0, v[10:11]
	v_lshl_add_u64 v[10:11], v[10:11], 0, v[206:207]
	global_store_dwordx2 v[10:11], v[54:55], off
	s_waitcnt lgkmcnt(0)
	v_mul_f32_e32 v10, 0x3b800000, v12
	v_pk_mul_f32 v[56:57], v[178:179], v[10:11] op_sel_hi:[1,0]
	v_pk_mul_f32 v[54:55], v[180:181], v[10:11] op_sel_hi:[1,0]
	v_pk_mul_f32 v[58:59], v[176:177], v[10:11] op_sel_hi:[1,0]
	v_pk_mul_f32 v[60:61], v[174:175], v[10:11] op_sel_hi:[1,0]
	v_pk_mul_f32 v[62:63], v[184:185], v[10:11] op_sel_hi:[1,0]
	v_pk_mul_f32 v[64:65], v[182:183], v[10:11] op_sel_hi:[1,0]
	v_mul_f32_e32 v11, 0xbfb8aa3b, v56
	v_exp_f32_e32 v11, v11
	v_mul_f32_e32 v12, 0xbfb8aa3b, v57
	v_exp_f32_e32 v12, v12
	v_pk_mul_f32 v[52:53], v[52:53], v[10:11] op_sel_hi:[1,0]
	v_add_f32_e32 v11, 1.0, v11
	v_rcp_f32_e32 v66, v11
	v_pk_mul_f32 v[10:11], v[50:51], v[10:11] op_sel_hi:[1,0]
	v_mul_f32_e32 v51, 0xbfb8aa3b, v54
	v_exp_f32_e32 v51, v51
	v_mul_f32_e32 v50, v56, v66
	v_mul_f32_e32 v56, 0xbfb8aa3b, v55
	v_exp_f32_e32 v56, v56
	v_add_f32_e32 v12, 1.0, v12
	v_rcp_f32_e32 v12, v12
	v_add_f32_e32 v51, 1.0, v51
	v_rcp_f32_e32 v51, v51
	v_add_f32_e32 v56, 1.0, v56
	v_rcp_f32_e32 v56, v56
	v_mul_f32_e32 v50, v64, v50
	v_mul_f32_e32 v12, v57, v12
	v_mul_f32_e32 v50, 0x41000000, v50
	v_mul_f32_e32 v12, v65, v12
	v_mul_f32_e32 v51, v54, v51
	v_mul_f32_e32 v12, 0x41000000, v12
	v_mul_f32_e32 v51, v62, v51
	v_mul_f32_e32 v54, v55, v56
	v_min_f32_e64 v55, |v50|, s33
	v_mul_f32_e32 v51, 0x41000000, v51
	v_mul_f32_e32 v54, v63, v54
	v_bfi_b32 v55, s2, v55, v50
	v_min_f32_e64 v50, |v12|, s33
	v_mul_f32_e32 v56, 0xbfb8aa3b, v60
	v_mul_f32_e32 v54, 0x41000000, v54
	v_bfi_b32 v12, s2, v50, v12
	v_min_f32_e64 v50, |v51|, s33
	v_exp_f32_e32 v56, v56
	v_bfi_b32 v51, s2, v50, v51
	v_min_f32_e64 v50, |v54|, s33
	v_bfi_b32 v54, s2, v50, v54
	v_mov_b32_e32 v50, v207
	v_cvt_pk_fp8_f32 v50, v55, v12
	v_mul_f32_e32 v12, 0xbfb8aa3b, v61
	v_exp_f32_e32 v12, v12
	v_add_f32_e32 v55, 1.0, v56
	v_rcp_f32_e32 v55, v55
	v_cvt_pk_fp8_f32 v50, v51, v54 op_sel:[0,0,1]
	v_add_f32_e32 v12, 1.0, v12
	v_rcp_f32_e32 v12, v12
	v_mul_f32_e32 v51, v60, v55
	v_mul_f32_e32 v10, v10, v51
	v_mul_f32_e32 v51, 0xbfb8aa3b, v58
	v_exp_f32_e32 v51, v51
	v_mul_f32_e32 v12, v61, v12
	v_mul_f32_e32 v11, v11, v12
	v_mul_f32_e32 v12, 0xbfb8aa3b, v59
	v_exp_f32_e32 v12, v12
	v_add_f32_e32 v51, 1.0, v51
	v_rcp_f32_e32 v51, v51
	v_mul_f32_e32 v10, 0x41000000, v10
	v_add_f32_e32 v12, 1.0, v12
	v_rcp_f32_e32 v12, v12
	v_mul_f32_e32 v51, v58, v51
	v_mul_f32_e32 v51, v52, v51
	v_mul_f32_e32 v11, 0x41000000, v11
	v_mul_f32_e32 v52, 0x41000000, v51
	v_min_f32_e64 v51, |v10|, s33
	v_bfi_b32 v10, s2, v51, v10
	v_min_f32_e64 v51, |v11|, s33
	v_mul_f32_e32 v12, v59, v12
	v_bfi_b32 v11, s2, v51, v11
	v_mov_b32_e32 v51, v207
	v_mul_f32_e32 v12, v53, v12
	v_cvt_pk_fp8_f32 v51, v10, v11
	v_mul_f32_e32 v12, 0x41000000, v12
	v_min_f32_e64 v53, |v52|, s33
	v_min_f32_e64 v11, |v12|, s33
	v_bfi_b32 v10, s2, v53, v52
	v_bfi_b32 v11, s2, v11, v12
	v_cvt_pk_fp8_f32 v51, v10, v11 op_sel:[0,0,1]
	v_add_co_u32_e32 v10, vcc, s0, v114
	s_mov_b32 s0, 0x48000
	s_nop 0
	v_addc_co_u32_e32 v11, vcc, 0, v115, vcc
	global_store_dwordx2 v[10:11], v[50:51], off
	v_mul_f32_e32 v10, 0x3b800000, v13
	v_pk_mul_f32 v[42:43], v[42:43], v[10:11] op_sel_hi:[1,0]
	v_pk_mul_f32 v[12:13], v[44:45], v[10:11] op_sel_hi:[1,0]
	v_pk_mul_f32 v[40:41], v[40:41], v[10:11] op_sel_hi:[1,0]
	v_pk_mul_f32 v[38:39], v[38:39], v[10:11] op_sel_hi:[1,0]
	v_pk_mul_f32 v[44:45], v[48:49], v[10:11] op_sel_hi:[1,0]
	v_pk_mul_f32 v[46:47], v[46:47], v[10:11] op_sel_hi:[1,0]
	v_mul_f32_e32 v11, 0xbfb8aa3b, v42
	v_exp_f32_e32 v11, v11
	v_mul_f32_e32 v48, 0xbfb8aa3b, v43
	v_exp_f32_e32 v48, v48
	v_pk_mul_f32 v[36:37], v[36:37], v[10:11] op_sel_hi:[1,0]
	v_add_f32_e32 v11, 1.0, v11
	v_rcp_f32_e32 v49, v11
	v_pk_mul_f32 v[10:11], v[34:35], v[10:11] op_sel_hi:[1,0]
	v_add_f32_e32 v34, 1.0, v48
	v_rcp_f32_e32 v34, v34
	v_mul_f32_e32 v35, v42, v49
	v_mul_f32_e32 v42, 0xbfb8aa3b, v12
	v_exp_f32_e32 v42, v42
	v_mul_f32_e32 v34, v43, v34
	v_mul_f32_e32 v43, 0xbfb8aa3b, v13
	v_exp_f32_e32 v43, v43
	v_add_f32_e32 v42, 1.0, v42
	v_rcp_f32_e32 v42, v42
	v_mul_f32_e32 v35, v46, v35
	v_add_f32_e32 v43, 1.0, v43
	v_rcp_f32_e32 v43, v43
	v_mul_f32_e32 v35, 0x41000000, v35
	v_mul_f32_e32 v34, v47, v34
	v_mul_f32_e32 v12, v12, v42
	v_mul_f32_e32 v34, 0x41000000, v34
	v_mul_f32_e32 v12, v44, v12
	v_mul_f32_e32 v13, v13, v43
	v_min_f32_e64 v42, |v35|, s33
	v_mul_f32_e32 v12, 0x41000000, v12
	v_mul_f32_e32 v13, v45, v13
	v_bfi_b32 v35, s2, v42, v35
	v_min_f32_e64 v42, |v34|, s33
	v_mul_f32_e32 v13, 0x41000000, v13
	v_bfi_b32 v34, s2, v42, v34
	v_min_f32_e64 v42, |v12|, s33
	v_bfi_b32 v42, s2, v42, v12
	v_min_f32_e64 v12, |v13|, s33
	v_bfi_b32 v13, s2, v12, v13
	v_mov_b32_e32 v12, v207
	v_cvt_pk_fp8_f32 v12, v35, v34
	v_mul_f32_e32 v34, 0xbfb8aa3b, v39
	v_exp_f32_e32 v34, v34
	v_mul_f32_e32 v43, 0xbfb8aa3b, v38
	v_exp_f32_e32 v43, v43
	v_cvt_pk_fp8_f32 v12, v42, v13 op_sel:[0,0,1]
	v_add_f32_e32 v13, 1.0, v34
	v_rcp_f32_e32 v13, v13
	v_add_f32_e32 v35, 1.0, v43
	v_rcp_f32_e32 v35, v35
	v_mul_f32_e32 v13, v39, v13
	v_mul_f32_e32 v11, v11, v13
	v_mul_f32_e32 v13, 0xbfb8aa3b, v41
	v_exp_f32_e32 v13, v13
	v_mul_f32_e32 v34, v38, v35
	v_mul_f32_e32 v10, v10, v34
	v_mul_f32_e32 v34, 0xbfb8aa3b, v40
	v_exp_f32_e32 v34, v34
	v_add_f32_e32 v13, 1.0, v13
	v_rcp_f32_e32 v13, v13
	v_mul_f32_e32 v10, 0x41000000, v10
	v_add_f32_e32 v34, 1.0, v34
	v_rcp_f32_e32 v34, v34
	v_mul_f32_e32 v13, v41, v13
	v_mul_f32_e32 v13, v37, v13
	v_mul_f32_e32 v11, 0x41000000, v11
	v_mul_f32_e32 v35, 0x41000000, v13
	v_min_f32_e64 v13, |v10|, s33
	v_bfi_b32 v10, s2, v13, v10
	v_min_f32_e64 v13, |v11|, s33
	v_mul_f32_e32 v34, v40, v34
	v_bfi_b32 v11, s2, v13, v11
	v_mov_b32_e32 v13, v207
	v_mul_f32_e32 v34, v36, v34
	v_cvt_pk_fp8_f32 v13, v10, v11
	v_mul_f32_e32 v34, 0x41000000, v34
	v_min_f32_e64 v36, |v34|, s33
	v_min_f32_e64 v11, |v35|, s33
	v_bfi_b32 v10, s2, v36, v34
	v_bfi_b32 v11, s2, v11, v35
	v_cvt_pk_fp8_f32 v13, v10, v11 op_sel:[0,0,1]
	ds_read2_b32 v[10:11], v132 offset0:160 offset1:176
	v_add_co_u32_e32 v34, vcc, s0, v114
	s_mov_b32 s0, 0x50000
	s_nop 0
	v_addc_co_u32_e32 v35, vcc, 0, v115, vcc
	s_waitcnt lgkmcnt(0)
	v_mul_f32_e32 v10, 0x3b800000, v10
	v_pk_mul_f32 v[26:27], v[26:27], v[10:11] op_sel_hi:[1,0]
	global_store_dwordx2 v[34:35], v[12:13], off
	v_pk_mul_f32 v[12:13], v[28:29], v[10:11] op_sel_hi:[1,0]
	v_pk_mul_f32 v[28:29], v[32:33], v[10:11] op_sel_hi:[1,0]
	v_mul_f32_e32 v32, 0xbfb8aa3b, v26
	v_mul_f32_e32 v33, 0xbfb8aa3b, v27
	v_exp_f32_e32 v32, v32
	v_exp_f32_e32 v33, v33
	v_pk_mul_f32 v[24:25], v[24:25], v[10:11] op_sel_hi:[1,0]
	v_pk_mul_f32 v[22:23], v[22:23], v[10:11] op_sel_hi:[1,0]
	v_pk_mul_f32 v[30:31], v[30:31], v[10:11] op_sel_hi:[1,0]
	v_pk_mul_f32 v[20:21], v[20:21], v[10:11] op_sel_hi:[1,0]
	v_add_f32_e32 v32, 1.0, v32
	v_pk_mul_f32 v[18:19], v[18:19], v[10:11] op_sel_hi:[1,0]
	v_add_f32_e32 v10, 1.0, v33
	v_rcp_f32_e32 v32, v32
	v_rcp_f32_e32 v10, v10
	v_mul_f32_e32 v26, v26, v32
	v_mul_f32_e32 v10, v27, v10
	v_mul_f32_e32 v27, 0xbfb8aa3b, v12
	v_mul_f32_e32 v26, v30, v26
	v_exp_f32_e32 v27, v27
	v_mul_f32_e32 v30, 0xbfb8aa3b, v13
	v_exp_f32_e32 v30, v30
	v_mul_f32_e32 v26, 0x41000000, v26
	v_add_f32_e32 v27, 1.0, v27
	v_rcp_f32_e32 v27, v27
	v_add_f32_e32 v30, 1.0, v30
	v_rcp_f32_e32 v30, v30
	v_mul_f32_e32 v10, v31, v10
	v_mul_f32_e32 v12, v12, v27
	v_mul_f32_e32 v10, 0x41000000, v10
	v_mul_f32_e32 v12, v28, v12
	v_mul_f32_e32 v13, v13, v30
	v_min_f32_e64 v27, |v26|, s33
	v_mul_f32_e32 v12, 0x41000000, v12
	v_mul_f32_e32 v13, v29, v13
	v_bfi_b32 v26, s2, v27, v26
	v_min_f32_e64 v27, |v10|, s33
	v_mul_f32_e32 v13, 0x41000000, v13
	v_bfi_b32 v10, s2, v27, v10
	v_min_f32_e64 v27, |v12|, s33
	v_mul_f32_e32 v28, 0xbfb8aa3b, v22
	v_bfi_b32 v27, s2, v27, v12
	v_min_f32_e64 v12, |v13|, s33
	v_exp_f32_e32 v28, v28
	v_bfi_b32 v13, s2, v12, v13
	v_mov_b32_e32 v12, v207
	v_cvt_pk_fp8_f32 v12, v26, v10
	v_mul_f32_e32 v10, 0xbfb8aa3b, v23
	v_exp_f32_e32 v10, v10
	v_add_f32_e32 v26, 1.0, v28
	v_rcp_f32_e32 v26, v26
	v_cvt_pk_fp8_f32 v12, v27, v13 op_sel:[0,0,1]
	v_add_f32_e32 v10, 1.0, v10
	v_rcp_f32_e32 v10, v10
	v_mul_f32_e32 v13, v22, v26
	v_mul_f32_e32 v13, v18, v13
	v_mul_f32_e32 v18, 0xbfb8aa3b, v24
	v_exp_f32_e32 v18, v18
	v_mul_f32_e32 v10, v23, v10
	v_mul_f32_e32 v10, v19, v10
	v_mul_f32_e32 v19, 0xbfb8aa3b, v25
	v_exp_f32_e32 v19, v19
	v_add_f32_e32 v18, 1.0, v18
	v_rcp_f32_e32 v18, v18
	v_mul_f32_e32 v13, 0x41000000, v13
	v_add_f32_e32 v19, 1.0, v19
	v_rcp_f32_e32 v19, v19
	v_mul_f32_e32 v18, v24, v18
	v_mul_f32_e32 v10, 0x41000000, v10
	v_mul_f32_e32 v18, v20, v18
	v_min_f32_e64 v20, |v13|, s33
	v_bfi_b32 v20, s2, v20, v13
	v_min_f32_e64 v13, |v10|, s33
	v_mul_f32_e32 v19, v25, v19
	v_bfi_b32 v10, s2, v13, v10
	v_mov_b32_e32 v13, v207
	v_mul_f32_e32 v18, 0x41000000, v18
	v_mul_f32_e32 v19, v21, v19
	v_cvt_pk_fp8_f32 v13, v20, v10
	v_mul_f32_e32 v19, 0x41000000, v19
	v_min_f32_e64 v21, |v18|, s33
	v_bfi_b32 v10, s2, v21, v18
	v_min_f32_e64 v18, |v19|, s33
	v_bfi_b32 v18, s2, v18, v19
	v_cvt_pk_fp8_f32 v13, v10, v18 op_sel:[0,0,1]
	v_add_co_u32_e32 v18, vcc, s0, v114
	v_mul_f32_e32 v10, 0x3b800000, v11
	s_nop 0
	v_addc_co_u32_e32 v19, vcc, 0, v115, vcc
	global_store_dwordx2 v[18:19], v[12:13], off
	v_pk_mul_f32 v[18:19], v[170:171], v[10:11] op_sel_hi:[1,0]
	v_pk_mul_f32 v[12:13], v[172:173], v[10:11] op_sel_hi:[1,0]
	v_pk_mul_f32 v[8:9], v[8:9], v[10:11] op_sel_hi:[1,0]
	v_pk_mul_f32 v[6:7], v[6:7], v[10:11] op_sel_hi:[1,0]
	v_pk_mul_f32 v[16:17], v[16:17], v[10:11] op_sel_hi:[1,0]
	v_pk_mul_f32 v[14:15], v[14:15], v[10:11] op_sel_hi:[1,0]
	v_mul_f32_e32 v11, 0xbfb8aa3b, v18
	v_exp_f32_e32 v11, v11
	v_mul_f32_e32 v20, 0xbfb8aa3b, v19
	v_exp_f32_e32 v20, v20
	s_mov_b64 s[0:1], -1
	v_pk_mul_f32 v[4:5], v[4:5], v[10:11] op_sel_hi:[1,0]
	v_add_f32_e32 v11, 1.0, v11
	v_rcp_f32_e32 v11, v11
	s_nop 0
	v_pk_mul_f32 v[2:3], v[2:3], v[10:11] op_sel_hi:[1,0]
	v_add_f32_e32 v10, 1.0, v20
	v_rcp_f32_e32 v10, v10
	v_mul_f32_e32 v11, v18, v11
	v_mul_f32_e32 v11, v14, v11
	v_mul_f32_e32 v14, 0xbfb8aa3b, v12
	v_mul_f32_e32 v10, v19, v10
	v_exp_f32_e32 v14, v14
	v_mul_f32_e32 v10, v15, v10
	v_mul_f32_e32 v15, 0xbfb8aa3b, v13
	v_exp_f32_e32 v15, v15
	v_add_f32_e32 v14, 1.0, v14
	v_rcp_f32_e32 v14, v14
	v_mul_f32_e32 v11, 0x41000000, v11
	v_add_f32_e32 v15, 1.0, v15
	v_rcp_f32_e32 v15, v15
	v_mul_f32_e32 v12, v12, v14
	v_mul_f32_e32 v10, 0x41000000, v10
	v_mul_f32_e32 v12, v16, v12
	v_mul_f32_e32 v13, v13, v15
	v_min_f32_e64 v14, |v11|, s33
	v_mul_f32_e32 v12, 0x41000000, v12
	v_mul_f32_e32 v13, v17, v13
	v_bfi_b32 v11, s2, v14, v11
	v_min_f32_e64 v14, |v10|, s33
	v_mul_f32_e32 v13, 0x41000000, v13
	v_bfi_b32 v14, s2, v14, v10
	v_min_f32_e64 v10, |v12|, s33
	v_bfi_b32 v12, s2, v10, v12
	v_min_f32_e64 v10, |v13|, s33
	v_bfi_b32 v13, s2, v10, v13
	v_mov_b32_e32 v10, v207
	v_mul_f32_e32 v15, 0xbfb8aa3b, v6
	v_exp_f32_e32 v15, v15
	v_cvt_pk_fp8_f32 v10, v11, v14
	v_mul_f32_e32 v11, 0xbfb8aa3b, v7
	v_exp_f32_e32 v11, v11
	v_add_f32_e32 v14, 1.0, v15
	v_rcp_f32_e32 v14, v14
	v_cvt_pk_fp8_f32 v10, v12, v13 op_sel:[0,0,1]
	v_add_f32_e32 v11, 1.0, v11
	v_rcp_f32_e32 v11, v11
	v_mul_f32_e32 v6, v6, v14
	v_mul_f32_e32 v2, v2, v6
	v_mul_f32_e32 v2, 0x41000000, v2
	v_mul_f32_e32 v6, v7, v11
	v_mul_f32_e32 v3, v3, v6
	v_mul_f32_e32 v6, 0xbfb8aa3b, v9
	v_exp_f32_e32 v6, v6
	v_mul_f32_e32 v7, 0xbfb8aa3b, v8
	v_exp_f32_e32 v7, v7
	v_mul_f32_e32 v3, 0x41000000, v3
	v_add_f32_e32 v6, 1.0, v6
	v_rcp_f32_e32 v6, v6
	v_add_f32_e32 v7, 1.0, v7
	v_rcp_f32_e32 v7, v7
	v_mov_b32_e32 v11, v207
	v_mul_f32_e32 v6, v9, v6
	v_mul_f32_e32 v5, v5, v6
	v_min_f32_e64 v6, |v2|, s33
	v_bfi_b32 v2, s2, v6, v2
	v_min_f32_e64 v6, |v3|, s33
	v_mul_f32_e32 v7, v8, v7
	v_bfi_b32 v3, s2, v6, v3
	v_mul_f32_e32 v4, v4, v7
	v_cvt_pk_fp8_f32 v11, v2, v3
	v_mul_f32_e32 v4, 0x41000000, v4
	v_mul_f32_e32 v5, 0x41000000, v5
	v_min_f32_e64 v6, |v4|, s33
	v_min_f32_e64 v3, |v5|, s33
	v_bfi_b32 v2, s2, v6, v4
	v_bfi_b32 v3, s2, v3, v5
	v_cvt_pk_fp8_f32 v11, v2, v3 op_sel:[0,0,1]
	v_add_co_u32_e32 v2, vcc, 0x58000, v114
	s_nop 1
	v_addc_co_u32_e32 v3, vcc, 0, v115, vcc
	s_and_b64 vcc, exec, s[38:39]
	global_store_dwordx2 v[2:3], v[10:11], off
	s_cmp_lt_i32 s100, 0
	s_cbranch_scc1 .Lfz_e_skip
	v_readlane_b32 s4, v253, 0
	v_readlane_b32 s5, v253, 1
	s_lshr_b32 s73, s100, 9
	s_mul_i32 s74, s73, 0xaaab
	s_lshr_b32 s74, s74, 17
	s_mul_i32 s75, s74, 3
	s_sub_i32 s73, s73, s75
	s_load_dwordx2 s[4:5], s[4:5], 0xa0
	v_readlane_b32 s23, v255, 55
	s_and_b32 s101, s100, 0x1ff
	s_add_i32 s23, s23, 1
	s_lshl_b32 s75, s23, 27
	s_lshl_b32 s100, s74, 22
	s_add_i32 s75, s75, s100
	s_and_b32 s100, s101, 31
	s_lshl_b32 s100, s100, 17
	s_add_i32 s75, s75, s100
	s_lshl_b32 s100, s73, 15
	s_add_i32 s75, s75, s100
	s_lshr_b32 s100, s101, 5
	s_lshl_b32 s100, s100, 6
	s_add_i32 s75, s75, s100
	s_add_u32 s75, s75, 0x3900000
	s_lshl_b32 s23, s23, 26
	s_lshl_b32 s74, s74, 21
	s_add_i32 s23, s23, s74
	s_and_b32 s74, s101, 15
	s_lshl_b32 s74, s74, 17
	s_add_i32 s23, s23, s74
	s_lshr_b32 s74, s101, 4
	s_lshl_b32 s74, s74, 6
	s_add_i32 s23, s23, s74
	s_add_u32 s23, s23, 0x23900000
	s_cmp_lt_u32 s73, 2
	s_cselect_b32 s75, s75, s23
	s_cselect_b32 s74, 12, 13
	s_mov_b32 s101, 0x800
	s_cselect_b32 s101, 0x400, s101
	s_mov_b32 s23, 0
	s_cselect_b32 s23, 0x8000, s23
	v_and_b32_e32 v224, 15, v0
	v_bfe_u32 v225, v0, 4, 2
	v_lshlrev_b32_e32 v202, s74, v224
	v_lshrrev_b32_e32 v224, 3, v224
	v_mul_u32_u24_e32 v224, s23, v224
	v_lshlrev_b32_e32 v225, 4, v225
	v_add3_u32 v202, v202, v224, v225
	v_mov_b32_e32 v204, 0x42800000
	v_mov_b32_e32 v205, 0x42800000
	v_mov_b32_e32 v203, 0xc3e00000
	s_waitcnt lgkmcnt(0)
	s_add_u32 s4, s4, s75
	s_addc_u32 s5, s5, 0
	s_waitcnt vmcnt(8)
	v_pk_mul_f32 v[134:135], v[134:135], v[204:205]
	v_pk_mul_f32 v[136:137], v[136:137], v[204:205]
	v_pk_mul_f32 v[138:139], v[138:139], v[204:205]
	v_pk_mul_f32 v[140:141], v[140:141], v[204:205]
	v_pk_mul_f32 v[142:143], v[142:143], v[204:205]
	v_pk_mul_f32 v[144:145], v[144:145], v[204:205]
	v_pk_mul_f32 v[146:147], v[146:147], v[204:205]
	v_pk_mul_f32 v[148:149], v[148:149], v[204:205]
	v_pk_mul_f32 v[150:151], v[150:151], v[204:205]
	v_pk_mul_f32 v[152:153], v[152:153], v[204:205]
	v_pk_mul_f32 v[154:155], v[154:155], v[204:205]
	v_pk_mul_f32 v[156:157], v[156:157], v[204:205]
	v_pk_mul_f32 v[158:159], v[158:159], v[204:205]
	v_pk_mul_f32 v[160:161], v[160:161], v[204:205]
	v_pk_mul_f32 v[162:163], v[162:163], v[204:205]
	v_pk_mul_f32 v[164:165], v[164:165], v[204:205]
	v_pk_mul_f32 v[166:167], v[166:167], v[204:205]
	v_pk_mul_f32 v[168:169], v[168:169], v[204:205]
	v_pk_mul_f32 v[186:187], v[186:187], v[204:205]
	v_pk_mul_f32 v[188:189], v[188:189], v[204:205]
	v_pk_mul_f32 v[190:191], v[190:191], v[204:205]
	v_pk_mul_f32 v[192:193], v[192:193], v[204:205]
	v_pk_mul_f32 v[208:209], v[208:209], v[204:205]
	v_pk_mul_f32 v[210:211], v[210:211], v[204:205]
	v_pk_mul_f32 v[212:213], v[212:213], v[204:205]
	v_pk_mul_f32 v[214:215], v[214:215], v[204:205]
	v_pk_mul_f32 v[216:217], v[216:217], v[204:205]
	v_pk_mul_f32 v[218:219], v[218:219], v[204:205]
	v_pk_mul_f32 v[220:221], v[220:221], v[204:205]
	v_pk_mul_f32 v[222:223], v[222:223], v[204:205]
	v_pk_mul_f32 v[234:235], v[234:235], v[204:205]
	v_pk_mul_f32 v[236:237], v[236:237], v[204:205]
	v_med3_f32 v134, v134, v203, s33
	v_med3_f32 v135, v135, v203, s33
	v_med3_f32 v136, v136, v203, s33
	v_med3_f32 v137, v137, v203, s33
	v_med3_f32 v138, v138, v203, s33
	v_med3_f32 v139, v139, v203, s33
	v_med3_f32 v140, v140, v203, s33
	v_med3_f32 v141, v141, v203, s33
	v_med3_f32 v142, v142, v203, s33
	v_med3_f32 v143, v143, v203, s33
	v_med3_f32 v144, v144, v203, s33
	v_med3_f32 v145, v145, v203, s33
	v_med3_f32 v146, v146, v203, s33
	v_med3_f32 v147, v147, v203, s33
	v_med3_f32 v148, v148, v203, s33
	v_med3_f32 v149, v149, v203, s33
	v_med3_f32 v150, v150, v203, s33
	v_med3_f32 v151, v151, v203, s33
	v_med3_f32 v152, v152, v203, s33
	v_med3_f32 v153, v153, v203, s33
	v_med3_f32 v154, v154, v203, s33
	v_med3_f32 v155, v155, v203, s33
	v_med3_f32 v156, v156, v203, s33
	v_med3_f32 v157, v157, v203, s33
	v_med3_f32 v158, v158, v203, s33
	v_med3_f32 v159, v159, v203, s33
	v_med3_f32 v160, v160, v203, s33
	v_med3_f32 v161, v161, v203, s33
	v_med3_f32 v162, v162, v203, s33
	v_med3_f32 v163, v163, v203, s33
	v_med3_f32 v164, v164, v203, s33
	v_med3_f32 v165, v165, v203, s33
	v_med3_f32 v166, v166, v203, s33
	v_med3_f32 v167, v167, v203, s33
	v_med3_f32 v168, v168, v203, s33
	v_med3_f32 v169, v169, v203, s33
	v_med3_f32 v186, v186, v203, s33
	v_med3_f32 v187, v187, v203, s33
	v_med3_f32 v188, v188, v203, s33
	v_med3_f32 v189, v189, v203, s33
	v_med3_f32 v190, v190, v203, s33
	v_med3_f32 v191, v191, v203, s33
	v_med3_f32 v192, v192, v203, s33
	v_med3_f32 v193, v193, v203, s33
	v_med3_f32 v208, v208, v203, s33
	v_med3_f32 v209, v209, v203, s33
	v_med3_f32 v210, v210, v203, s33
	v_med3_f32 v211, v211, v203, s33
	v_med3_f32 v212, v212, v203, s33
	v_med3_f32 v213, v213, v203, s33
	v_med3_f32 v214, v214, v203, s33
	v_med3_f32 v215, v215, v203, s33
	v_med3_f32 v216, v216, v203, s33
	v_med3_f32 v217, v217, v203, s33
	v_med3_f32 v218, v218, v203, s33
	v_med3_f32 v219, v219, v203, s33
	v_med3_f32 v220, v220, v203, s33
	v_med3_f32 v221, v221, v203, s33
	v_med3_f32 v222, v222, v203, s33
	v_med3_f32 v223, v223, v203, s33
	v_med3_f32 v234, v234, v203, s33
	v_med3_f32 v235, v235, v203, s33
	v_med3_f32 v236, v236, v203, s33
	v_med3_f32 v237, v237, v203, s33
	v_cvt_pk_fp8_f32 v242, v134, v138
	v_cvt_pk_fp8_f32 v243, v150, v154
	v_cvt_pk_fp8_f32 v244, v166, v186
	v_cvt_pk_fp8_f32 v245, v212, v216
	v_cvt_pk_fp8_f32 v242, v142, v146 op_sel:[0,0,1]
	v_cvt_pk_fp8_f32 v243, v158, v162 op_sel:[0,0,1]
	v_cvt_pk_fp8_f32 v244, v190, v208 op_sel:[0,0,1]
	v_cvt_pk_fp8_f32 v245, v220, v234 op_sel:[0,0,1]
	s_nop 1
	global_store_dwordx4 v202, v[242:245], s[4:5] nt
	s_add_u32 s4, s4, s101
	s_addc_u32 s5, s5, 0
	v_cvt_pk_fp8_f32 v246, v135, v139
	v_cvt_pk_fp8_f32 v247, v151, v155
	v_cvt_pk_fp8_f32 v248, v167, v187
	v_cvt_pk_fp8_f32 v249, v213, v217
	v_cvt_pk_fp8_f32 v246, v143, v147 op_sel:[0,0,1]
	v_cvt_pk_fp8_f32 v247, v159, v163 op_sel:[0,0,1]
	v_cvt_pk_fp8_f32 v248, v191, v209 op_sel:[0,0,1]
	v_cvt_pk_fp8_f32 v249, v221, v235 op_sel:[0,0,1]
	s_nop 1
	global_store_dwordx4 v202, v[246:249], s[4:5] nt
	s_add_u32 s4, s4, s101
	s_addc_u32 s5, s5, 0
	v_cvt_pk_fp8_f32 v242, v136, v140
	v_cvt_pk_fp8_f32 v243, v152, v156
	v_cvt_pk_fp8_f32 v244, v168, v188
	v_cvt_pk_fp8_f32 v245, v214, v218
	v_cvt_pk_fp8_f32 v242, v144, v148 op_sel:[0,0,1]
	v_cvt_pk_fp8_f32 v243, v160, v164 op_sel:[0,0,1]
	v_cvt_pk_fp8_f32 v244, v192, v210 op_sel:[0,0,1]
	v_cvt_pk_fp8_f32 v245, v222, v236 op_sel:[0,0,1]
	s_nop 1
	global_store_dwordx4 v202, v[242:245], s[4:5] nt
	s_add_u32 s4, s4, s101
	s_addc_u32 s5, s5, 0
	v_cvt_pk_fp8_f32 v246, v137, v141
	v_cvt_pk_fp8_f32 v247, v153, v157
	v_cvt_pk_fp8_f32 v248, v169, v189
	v_cvt_pk_fp8_f32 v249, v215, v219
	v_cvt_pk_fp8_f32 v246, v145, v149 op_sel:[0,0,1]
	v_cvt_pk_fp8_f32 v247, v161, v165 op_sel:[0,0,1]
	v_cvt_pk_fp8_f32 v248, v193, v211 op_sel:[0,0,1]
	v_cvt_pk_fp8_f32 v249, v223, v237 op_sel:[0,0,1]
	s_nop 1
	global_store_dwordx4 v202, v[246:249], s[4:5] nt
.Lfz_e_skip:
	s_cbranch_vccnz .LBB0_1242
	s_andn2_b64 vcc, exec, s[48:49]
	s_cbranch_vccnz .LBB0_1241
	s_barrier
	s_branch .LBB0_1241

	.amdhsa_kernel _Z8mega_fwd4Args
		.amdhsa_group_segment_fixed_size 0
		.amdhsa_private_segment_fixed_size 0
		.amdhsa_kernarg_size 432
		.amdhsa_user_sgpr_count 2
		.amdhsa_user_sgpr_dispatch_ptr 0
		.amdhsa_user_sgpr_queue_ptr 0
		.amdhsa_user_sgpr_kernarg_segment_ptr 1
		.amdhsa_user_sgpr_dispatch_id 0
		.amdhsa_user_sgpr_kernarg_preload_length 0
		.amdhsa_user_sgpr_kernarg_preload_offset 0
		.amdhsa_user_sgpr_private_segment_size 0
		.amdhsa_uses_dynamic_stack 0
		.amdhsa_enable_private_segment 0
		.amdhsa_system_sgpr_workgroup_id_x 1
		.amdhsa_system_sgpr_workgroup_id_y 0
		.amdhsa_system_sgpr_workgroup_id_z 0
		.amdhsa_system_sgpr_workgroup_info 0
		.amdhsa_system_vgpr_workitem_id 0
		.amdhsa_next_free_vgpr 256
		.amdhsa_next_free_sgpr 102
		.amdhsa_accum_offset 256
		.amdhsa_reserve_vcc 1
		.amdhsa_float_round_mode_32 0
		.amdhsa_float_round_mode_16_64 0
		.amdhsa_float_denorm_mode_32 3
		.amdhsa_float_denorm_mode_16_64 3
		.amdhsa_dx10_clamp 1
		.amdhsa_ieee_mode 1
		.amdhsa_fp16_overflow 0
		.amdhsa_tg_split 0
		.amdhsa_exception_fp_ieee_invalid_op 0
		.amdhsa_exception_fp_denorm_src 0
		.amdhsa_exception_fp_ieee_div_zero 0
		.amdhsa_exception_fp_ieee_overflow 0
		.amdhsa_exception_fp_ieee_underflow 0
		.amdhsa_exception_fp_ieee_inexact 0
		.amdhsa_exception_int_div_zero 0
	.end_amdhsa_kernel

amdhsa.kernels:
  - .agpr_count:     0
    .args:
      - .offset:         0
        .size:           176
        .value_kind:     by_value
      - .offset:         176
        .size:           4
        .value_kind:     hidden_block_count_x
      - .offset:         180
        .size:           4
        .value_kind:     hidden_block_count_y
      - .offset:         184
        .size:           4
        .value_kind:     hidden_block_count_z
      - .offset:         188
        .size:           2
        .value_kind:     hidden_group_size_x
      - .offset:         190
        .size:           2
        .value_kind:     hidden_group_size_y
      - .offset:         192
        .size:           2
        .value_kind:     hidden_group_size_z
      - .offset:         194
        .size:           2
        .value_kind:     hidden_remainder_x
      - .offset:         196
        .size:           2
        .value_kind:     hidden_remainder_y
      - .offset:         198
        .size:           2
        .value_kind:     hidden_remainder_z
      - .offset:         216
        .size:           8
        .value_kind:     hidden_global_offset_x
      - .offset:         224
        .size:           8
        .value_kind:     hidden_global_offset_y
      - .offset:         232
        .size:           8
        .value_kind:     hidden_global_offset_z
      - .offset:         240
        .size:           2
        .value_kind:     hidden_grid_dims
      - .offset:         296
        .size:           4
        .value_kind:     hidden_dynamic_lds_size
    .group_segment_fixed_size: 0
    .kernarg_segment_align: 8
    .kernarg_segment_size: 432
    .language:       OpenCL C
    .language_version:
      - 2
      - 0
    .max_flat_workgroup_size: 512
    .name:           _Z8mega_fwd4Args
    .private_segment_fixed_size: 0
    .sgpr_count:     108
    .sgpr_spill_count: 186
    .symbol:         _Z8mega_fwd4Args.kd
    .uniform_work_group_size: 1
    .uses_dynamic_stack: false
    .vgpr_count:     256
    .vgpr_spill_count: 0
    .wavefront_size: 64
